# v36
# baseline (speedup 1.0000x reference)
.LBB1_12:
	s_waitcnt vmcnt(8)
	s_waitcnt lgkmcnt(0)
	s_barrier
	v_mfma_f32_16x16x32_f16 v[128:131], v[148:151], v[166:169], v[128:131]
	v_mfma_f32_16x16x32_f16 v[128:131], v[152:155], v[174:177], v[128:131]
	v_mfma_f32_16x16x32_f16 v[120:123], v[160:163], v[174:177], v[120:123]
	v_mfma_f32_16x16x32_f16 v[120:123], v[156:159], v[166:169], v[120:123]
	v_mfma_f32_16x16x32_f16 v[104:107], v[156:159], v[170:173], v[104:107]
	v_mfma_f32_16x16x32_f16 v[104:107], v[160:163], v[178:181], v[104:107]
	v_mfma_f32_16x16x32_f16 v[112:115], v[152:155], v[178:181], v[112:115]
	v_mfma_f32_16x16x32_f16 v[112:115], v[148:151], v[170:173], v[112:115]
	v_mfma_f32_16x16x32_f16 v[96:99], v[148:151], v[182:185], v[96:99]
	v_mfma_f32_16x16x32_f16 v[96:99], v[152:155], v[190:193], v[96:99]
	v_mfma_f32_16x16x32_f16 v[88:91], v[160:163], v[190:193], v[88:91]
	v_mfma_f32_16x16x32_f16 v[88:91], v[156:159], v[182:185], v[88:91]
	v_mfma_f32_16x16x32_f16 v[72:75], v[156:159], v[186:189], v[72:75]
	v_mfma_f32_16x16x32_f16 v[72:75], v[160:163], v[214:217], v[72:75]
	v_mfma_f32_16x16x32_f16 v[80:83], v[152:155], v[214:217], v[80:83]
	v_mfma_f32_16x16x32_f16 v[80:83], v[148:151], v[186:189], v[80:83]
	v_mfma_f32_16x16x32_f16 v[124:127], v[132:135], v[166:169], v[124:127]
	v_mfma_f32_16x16x32_f16 v[124:127], v[136:139], v[174:177], v[124:127]
	v_mfma_f32_16x16x32_f16 v[116:119], v[144:147], v[174:177], v[116:119]
	v_mfma_f32_16x16x32_f16 v[116:119], v[140:143], v[166:169], v[116:119]
	v_mfma_f32_16x16x32_f16 v[100:103], v[140:143], v[170:173], v[100:103]
	v_mfma_f32_16x16x32_f16 v[100:103], v[144:147], v[178:181], v[100:103]
	v_mfma_f32_16x16x32_f16 v[108:111], v[136:139], v[178:181], v[108:111]
	v_mfma_f32_16x16x32_f16 v[108:111], v[132:135], v[170:173], v[108:111]
	v_mfma_f32_16x16x32_f16 v[92:95], v[132:135], v[182:185], v[92:95]
	v_mfma_f32_16x16x32_f16 v[92:95], v[136:139], v[190:193], v[92:95]
	v_mfma_f32_16x16x32_f16 v[84:87], v[144:147], v[190:193], v[84:87]
	v_mfma_f32_16x16x32_f16 v[84:87], v[140:143], v[182:185], v[84:87]
	v_mfma_f32_16x16x32_f16 v[68:71], v[140:143], v[186:189], v[68:71]
	v_mfma_f32_16x16x32_f16 v[68:71], v[144:147], v[214:217], v[68:71]
	v_mfma_f32_16x16x32_f16 v[76:79], v[136:139], v[214:217], v[76:79]
	v_mfma_f32_16x16x32_f16 v[76:79], v[132:135], v[186:189], v[76:79]
	s_barrier
	s_andn2_b64 vcc, exec, s[4:5]
	s_cbranch_vccnz .LBB1_16
	v_cvt_pkrtz_f16_f32 v166, v0, v1
	v_cvt_pkrtz_f16_f32 v167, v2, v3
	v_add_u32_e32 v166, 0x20002, v166
	v_add_u32_e32 v167, 0x20002, v167
	v_and_b32_e32 v166, 0xfffcfffc, v166
	v_and_b32_e32 v167, 0xfffcfffc, v167
	global_store_dwordx2 v231, v[166:167], s[90:91] sc1
